# stack on top of the epilogue/lookup/wait fixes: SB/MEM next-tile K/V loads after the Q re-read, map-1 P.V LDS reads pre-issued at the previous tail, one static s_setprio 1 for waves 4-7 in the diff-at
# speedup vs baseline: 1.0021x; 1.0014x over previous
.LBB0_634:
	s_or_b64 exec, exec, s[0:1]
	s_not_b32 s0, s9
	s_bfe_u32 s73, s2, 0x20006
	s_lshl_b32 s0, s0, 7
	s_ashr_i32 s10, s5, 3
	s_and_b32 s53, s0, 0x1f80
	s_lshl_b32 s0, s73, 5
	s_or_b32 s9, s0, s53
	s_and_b32 s0, s2, 0x3fffffc0
	s_ashr_i32 s11, s10, 31
	v_or_b32_e32 v1, s9, v180
	s_lshl_b32 s0, s0, 2
	s_lshl_b64 s[54:55], s[10:11], 13
	s_add_i32 s95, s0, 0
	v_or_b32_e32 v1, s54, v1
	v_mov_b64_e32 v[4:5], s[88:89]
	s_movk_i32 s0, 0x6880
	v_mad_u64_u32 v[4:5], s[0:1], v1, s0, v[4:5]
	s_lshr_b32 s13, s2, 8
	v_mad_i32_i24 v5, s55, v227, v5
	s_lshl_b32 s42, s4, 8
	v_lshl_add_u64 v[4:5], v[4:5], 0, s[42:43]
	s_lshl_b32 s0, s13, 7
	s_mov_b32 s1, s43
	s_lshr_b32 s12, s2, 6
	s_add_i32 s95, s95, 0x20800
	s_lshl_b32 s72, s4, 7
	v_lshl_add_u64 v[4:5], v[4:5], 0, s[0:1]
	s_mul_i32 s1, s10, 0xd100000
	s_mul_hi_i32 s14, s10, 0xd100000
	s_add_u32 s4, s88, s1
	s_addc_u32 s5, s89, s14
	s_add_u32 s4, s4, s42
	s_addc_u32 s5, s5, 0
	s_lshl_b32 s15, s12, 3
	s_lshr_b32 s10, s2, 4
	v_or_b32_e32 v6, s15, v193
	s_and_b32 s16, s10, 4
	v_mad_u64_u32 v[6:7], s[10:11], v6, s94, v[200:201]
	v_or_b32_e32 v7, s15, v221
	v_bitop3_b32 v1, s15, v228, v218 bitop3:0xc8
	v_mad_u64_u32 v[8:9], s[10:11], v7, s94, v[202:203]
	v_mov_b32_e32 v7, v3
	v_or3_b32 v2, v219, v1, s16
	s_lshl_b32 s10, s12, 11
	v_lshlrev_b64 v[6:7], 1, v[6:7]
	v_mul_lo_u32 v2, v2, s94
	v_lshl_add_u64 v[12:13], s[4:5], 0, v[6:7]
	s_mov_b64 s[18:19], 0x800
	s_add_i32 s52, s10, 0
	v_or_b32_e32 v2, v2, v223
	v_lshl_add_u64 v[12:13], v[12:13], 0, s[18:19]
	s_mov_b32 m0, s52
	s_mov_b64 s[10:11], 0x1000
	global_load_lds_dwordx4 v[12:13], off
	v_lshlrev_b64 v[12:13], 1, v[2:3]
	v_lshl_add_u64 v[14:15], s[4:5], 0, v[12:13]
	v_mov_b32_e32 v9, v3
	v_lshl_add_u64 v[16:17], v[14:15], 0, s[10:11]
	s_add_i32 m0, s52, 0x4000
	v_lshlrev_b64 v[8:9], 1, v[8:9]
	global_load_lds_dwordx4 v[16:17], off
	v_lshl_add_u64 v[16:17], s[4:5], 0, v[8:9]
	v_lshl_add_u64 v[16:17], v[16:17], 0, s[18:19]
	s_add_i32 m0, s52, 0x400
	s_addk_i32 s53, 0x80
	global_load_lds_dwordx4 v[16:17], off
	s_mov_b64 s[10:11], 0x1080
	s_add_i32 m0, s52, 0x4400
	v_lshl_add_u64 v[14:15], v[14:15], 0, s[10:11]
	s_add_u32 s10, s4, 0x1a2800
	s_addc_u32 s11, s5, 0
	s_add_u32 s4, s4, 0x1a3000
	global_load_lds_dwordx4 v[14:15], off
	s_addc_u32 s5, s5, 0
	v_lshl_add_u64 v[6:7], s[10:11], 0, v[6:7]
	s_add_i32 m0, s52, 0x8000
	v_add_u32_e32 v10, 64, v2
	global_load_lds_dwordx4 v[6:7], off
	v_lshl_add_u64 v[6:7], s[4:5], 0, v[12:13]
	s_add_i32 m0, s52, 0xc000
	v_mov_b32_e32 v11, v3
	global_load_lds_dwordx4 v[6:7], off
	v_lshl_add_u64 v[6:7], s[10:11], 0, v[8:9]
	s_add_i32 m0, s52, 0x8400
	v_lshlrev_b32_e32 v2, 1, v182
	global_load_lds_dwordx4 v[6:7], off
	v_lshl_add_u64 v[6:7], v[10:11], 1, s[4:5]
	s_add_i32 m0, s52, 0xc400
	v_lshl_add_u64 v[4:5], v[4:5], 0, v[2:3]
	global_load_lds_dwordx4 v[6:7], off
	global_load_dwordx4 v[132:135], v[4:5], off
	global_load_dwordx4 v[136:139], v[4:5], off offset:32
	global_load_dwordx4 v[140:143], v[4:5], off offset:64
	global_load_dwordx4 v[144:147], v[4:5], off offset:96
	s_lshr_b32 s76, s53, 6
	s_cmp_eq_u32 s13, 1
	s_cselect_b64 s[56:57], -1, 0
	s_cmpk_lt_u32 s2, 0x100
	v_or_b32_e32 v2, s0, v183
	s_cselect_b64 s[58:59], -1, 0
	v_bitop3_b32 v234, s0, v186, v183 bitop3:0x36
	s_movk_i32 s0, 0x60
	s_sub_i32 s77, 0xb0, s9
	s_or_b32 s2, s1, s42
	v_add3_u32 v1, v219, v1, s16
	v_bitop3_b32 v237, v2, v186, s0 bitop3:0x36
	v_mul_lo_u32 v1, v1, s94
	s_add_u32 s0, s92, s2
	v_bitop3_b32 v235, v2, v186, 32 bitop3:0x36
	v_bitop3_b32 v236, v2, v186, 64 bitop3:0x36
	v_or_b32_e32 v2, v223, v1
	s_addc_u32 s1, s93, s14
	v_lshl_add_u64 v[206:207], v[2:3], 1, s[0:1]
	s_mul_i32 s12, s12, 0x1a200
	s_add_u32 s0, s84, s2
	v_add_u32_e32 v2, s12, v224
	s_addc_u32 s1, s97, s14
	v_lshl_add_u64 v[208:209], v[2:3], 1, s[0:1]
	v_add_u32_e32 v2, s12, v225
	v_mov_b32_e32 v16, v3
	v_mov_b32_e32 v17, v3
	v_lshl_add_u64 v[210:211], v[2:3], 1, s[0:1]
	v_mov_b32_e32 v2, v3
	v_mov_b32_e32 v4, v3
	v_mov_b32_e32 v5, v3
	v_mov_b32_e32 v6, v3
	v_mov_b32_e32 v7, v3
	v_mov_b32_e32 v8, v3
	v_mov_b32_e32 v9, v3
	v_mov_b32_e32 v10, v3
	v_mov_b32_e32 v12, v3
	v_mov_b32_e32 v13, v3
	v_mov_b32_e32 v14, v3
	v_mov_b32_e32 v15, v3
	v_mov_b64_e32 v[66:67], v[16:17]
	v_mov_b64_e32 v[50:51], v[16:17]
	v_mov_b64_e32 v[34:35], v[16:17]
	v_mov_b64_e32 v[64:65], v[14:15]
	v_mov_b64_e32 v[62:63], v[12:13]
	v_mov_b64_e32 v[60:61], v[10:11]
	v_mov_b64_e32 v[58:59], v[8:9]
	v_mov_b64_e32 v[56:57], v[6:7]
	v_mov_b64_e32 v[54:55], v[4:5]
	v_mov_b64_e32 v[52:53], v[2:3]
	v_mov_b64_e32 v[48:49], v[14:15]
	v_mov_b64_e32 v[46:47], v[12:13]
	v_mov_b64_e32 v[44:45], v[10:11]
	v_mov_b64_e32 v[42:43], v[8:9]
	v_mov_b64_e32 v[40:41], v[6:7]
	v_mov_b64_e32 v[38:39], v[4:5]
	v_mov_b64_e32 v[36:37], v[2:3]
	v_mov_b64_e32 v[32:33], v[14:15]
	v_mov_b64_e32 v[30:31], v[12:13]
	v_mov_b64_e32 v[28:29], v[10:11]
	v_mov_b64_e32 v[26:27], v[8:9]
	v_mov_b64_e32 v[24:25], v[6:7]
	v_mov_b64_e32 v[22:23], v[4:5]
	v_mov_b64_e32 v[20:21], v[2:3]
	v_mov_b64_e32 v[18:19], v[16:17]
	s_mov_b32 s68, 2
	v_mov_b32_e32 v69, v68
	v_mov_b32_e32 v70, v68
	v_mov_b32_e32 v71, v68
	v_mov_b32_e32 v72, v68
	v_mov_b32_e32 v73, v68
	v_mov_b32_e32 v74, v68
	v_mov_b32_e32 v75, v68
	v_mov_b32_e32 v76, v68
	v_mov_b32_e32 v77, v68
	v_mov_b32_e32 v78, v68
	v_mov_b32_e32 v79, v68
	v_mov_b32_e32 v80, v68
	v_mov_b32_e32 v81, v68
	v_mov_b32_e32 v82, v68
	v_mov_b32_e32 v83, v68
	v_lshl_add_u32 v232, v180, 2, s95
	v_add_u32_e32 v238, s9, v226
	s_mov_b32 s42, 0
	v_mov_b32_e32 v233, 0
	s_mov_b32 s4, 0x10000
	s_mov_b64 s[60:61], 0
	v_mov_b32_e32 v84, 0
	v_mov_b32_e32 v85, 0
	v_mov_b32_e32 v86, 0
	v_mov_b32_e32 v87, 0
	v_mov_b32_e32 v88, 0
	v_mov_b32_e32 v89, 0
	v_mov_b32_e32 v90, 0
	v_mov_b32_e32 v91, 0
	v_mov_b32_e32 v92, 0
	v_mov_b32_e32 v93, 0
	v_mov_b32_e32 v94, 0
	v_mov_b32_e32 v95, 0
	v_mov_b32_e32 v96, 0
	v_mov_b32_e32 v97, 0
	v_mov_b32_e32 v98, 0
	v_mov_b32_e32 v99, 0
	v_mov_b64_e32 v[16:17], v[14:15]
	v_mov_b64_e32 v[14:15], v[12:13]
	v_mov_b64_e32 v[12:13], v[10:11]
	v_mov_b64_e32 v[10:11], v[8:9]
	v_mov_b64_e32 v[8:9], v[6:7]
	v_mov_b64_e32 v[6:7], v[4:5]
	v_mov_b64_e32 v[4:5], v[2:3]
	s_waitcnt vmcnt(0)
	s_and_b64 s[0:1], s[56:57], exec
	s_cbranch_scc0 .Lsp_skip
	s_setprio 1

.LBB0_721:
	s_setprio 0
	s_and_b64 vcc, exec, s[56:57]
	s_cbranch_vccz .LBB0_723
	s_lshl_b32 s0, s53, 9
	s_add_i32 s0, s0, 0x18000
	s_and_b32 s0, s0, 0x18000
	v_add_u32_e32 v1, s0, v222
	ds_read_b64_tr_b16 v[68:69], v1 offset:0
	ds_read_b64_tr_b16 v[70:71], v1 offset:0x800
	ds_read_b64_tr_b16 v[72:73], v1 offset:0x1000
	ds_read_b64_tr_b16 v[74:75], v1 offset:0x1800
	ds_read_b64_tr_b16 v[76:77], v1 offset:0x2000
	ds_read_b64_tr_b16 v[78:79], v1 offset:0x2800
	ds_read_b64_tr_b16 v[80:81], v1 offset:0x3000
	ds_read_b64_tr_b16 v[82:83], v1 offset:0x3800
	ds_read_b64_tr_b16 v[100:101], v1 offset:0x200
	ds_read_b64_tr_b16 v[102:103], v1 offset:0xa00
	ds_read_b64_tr_b16 v[104:105], v1 offset:0x1200
	ds_read_b64_tr_b16 v[106:107], v1 offset:0x1a00
	ds_read_b64_tr_b16 v[108:109], v1 offset:0x2200
	ds_read_b64_tr_b16 v[110:111], v1 offset:0x2a00
	ds_read_b64_tr_b16 v[112:113], v1 offset:0x3200
	ds_read_b64_tr_b16 v[114:115], v1 offset:0x3a00
	s_waitcnt lgkmcnt(8)
	s_nop 0
	v_mfma_f32_32x32x16_bf16 v[52:67], v[96:99], v[68:71], v[52:67]
	v_mfma_f32_32x32x16_bf16 v[52:67], v[92:95], v[72:75], v[52:67]
	v_mfma_f32_32x32x16_bf16 v[52:67], v[88:91], v[76:79], v[52:67]
	v_mfma_f32_32x32x16_bf16 v[52:67], v[84:87], v[80:83], v[52:67]
	ds_read_b64_tr_b16 v[68:69], v1 offset:0x400
	ds_read_b64_tr_b16 v[70:71], v1 offset:0xc00
	ds_read_b64_tr_b16 v[72:73], v1 offset:0x1400
	ds_read_b64_tr_b16 v[74:75], v1 offset:0x1c00
	ds_read_b64_tr_b16 v[76:77], v1 offset:0x2400
	ds_read_b64_tr_b16 v[78:79], v1 offset:0x2c00
	ds_read_b64_tr_b16 v[80:81], v1 offset:0x3400
	ds_read_b64_tr_b16 v[82:83], v1 offset:0x3c00
	s_waitcnt lgkmcnt(8)
	v_mfma_f32_32x32x16_bf16 v[36:51], v[96:99], v[100:103], v[36:51]
	v_mfma_f32_32x32x16_bf16 v[36:51], v[92:95], v[104:107], v[36:51]
	v_mfma_f32_32x32x16_bf16 v[36:51], v[88:91], v[108:111], v[36:51]
	v_mfma_f32_32x32x16_bf16 v[36:51], v[84:87], v[112:115], v[36:51]
	ds_read_b64_tr_b16 v[100:101], v1 offset:0x600
	ds_read_b64_tr_b16 v[102:103], v1 offset:0xe00
	ds_read_b64_tr_b16 v[104:105], v1 offset:0x1600
	ds_read_b64_tr_b16 v[106:107], v1 offset:0x1e00
	ds_read_b64_tr_b16 v[108:109], v1 offset:0x2600
	ds_read_b64_tr_b16 v[110:111], v1 offset:0x2e00
	ds_read_b64_tr_b16 v[112:113], v1 offset:0x3600
	ds_read_b64_tr_b16 v[114:115], v1 offset:0x3e00
	s_waitcnt lgkmcnt(8)
	v_mfma_f32_32x32x16_bf16 v[20:35], v[96:99], v[68:71], v[20:35]
	v_mfma_f32_32x32x16_bf16 v[20:35], v[92:95], v[72:75], v[20:35]
	v_mfma_f32_32x32x16_bf16 v[20:35], v[88:91], v[76:79], v[20:35]
	v_mfma_f32_32x32x16_bf16 v[20:35], v[84:87], v[80:83], v[20:35]
	s_waitcnt lgkmcnt(0)
	v_mfma_f32_32x32x16_bf16 v[4:19], v[96:99], v[100:103], v[4:19]
	v_mfma_f32_32x32x16_bf16 v[4:19], v[92:95], v[104:107], v[4:19]
	v_mfma_f32_32x32x16_bf16 v[4:19], v[88:91], v[108:111], v[4:19]
	v_mfma_f32_32x32x16_bf16 v[4:19], v[84:87], v[112:115], v[4:19]
